# M0 gather loop: counted vmcnt waits (5/4) so the row-copy stores stay in flight instead of being drained every row; on top of v040
# speedup vs baseline: 1.0059x; 1.0033x over previous
.LBB0_1418:
	s_or_b64 exec, exec, s[16:17]
	s_lshl_b32 s16, s22, 3
	s_add_i32 s18, s16, s20
	s_cmp_gt_i32 s18, 0x83ff
	s_cbranch_scc1 .LBB0_1427
	s_ashr_i32 s19, s18, 31
	s_lshl_b32 s8, s21, 3
	s_lshl_b64 s[10:11], s[18:19], 11
	s_add_u32 s10, s14, s10
	s_addc_u32 s11, s15, s11
	v_lshlrev_b32_e32 v2, 4, v1
	v_lshl_add_u64 v[8:9], s[10:11], 0, v[2:3]
	s_mov_b64 s[10:11], 0x18800000
	v_lshl_add_u64 v[4:5], v[8:9], 0, s[10:11]
	s_lshl_b64 s[10:11], s[18:19], 3
	s_add_u32 s22, s14, s10
	s_addc_u32 s23, s15, s11
	v_mov_b32_e32 v1, 0x480000
	global_load_dwordx4 v[4:7], v[4:5], off offset:1024
	s_mov_b32 s9, 0x18800000
	global_load_dwordx2 v[24:25], v1, s[22:23]
	s_lshl_b64 s[22:23], s[18:19], 2
	v_add_co_u32_e32 v8, vcc, s9, v8
	s_add_u32 s22, s14, s22
	s_nop 0
	v_addc_co_u32_e32 v9, vcc, 0, v9, vcc
	s_addc_u32 s23, s15, s23
	v_mov_b32_e32 v1, 0x400000
	global_load_dword v1, v1, s[22:23]
	s_nop 0
	global_load_dwordx4 v[8:11], v[8:9], off
	s_add_u32 s21, s10, 0x580000
	v_lshl_add_u64 v[12:13], s[14:15], 0, v[2:3]
	s_mov_b64 s[22:23], 0x1ca00000
	s_addc_u32 s26, s11, 0
	s_add_i32 s17, s20, s8
	v_lshl_add_u64 v[20:21], v[12:13], 0, s[22:23]
	s_add_i32 s22, s17, s16
	s_ashr_i32 s9, s8, 31
	s_ashr_i32 s23, s22, 31
	s_lshl_b64 s[10:11], s[8:9], 3
	s_lshl_b64 s[16:17], s[22:23], 2
	s_add_u32 s20, s16, 0x400000
	s_addc_u32 s27, s17, 0
	s_lshl_b64 s[16:17], s[8:9], 2
	s_lshl_b64 s[24:25], s[22:23], 3
	s_add_u32 s34, s24, 0x480000
	s_addc_u32 s35, s25, 0
	s_lshl_b64 s[24:25], s[22:23], 11
	s_lshl_b64 s[22:23], s[8:9], 11
	v_or_b32_e32 v22, s24, v2
	v_mov_b32_e32 v23, s25
	s_waitcnt vmcnt(3)
	v_mov_b64_e32 v[14:15], v[6:7]
	v_mov_b64_e32 v[12:13], v[4:5]
	s_waitcnt vmcnt(2)
	v_mov_b64_e32 v[26:27], v[24:25]
	s_waitcnt vmcnt(1)
	v_mov_b32_e32 v2, v1
	s_waitcnt vmcnt(0)
	v_mov_b64_e32 v[18:19], v[10:11]
	v_mov_b64_e32 v[16:17], v[8:9]
	s_branch .LBB0_1422
	s_branch .LBB0_1420
.Lm0_skiprow:
	s_waitcnt vmcnt(0)
	s_branch .LBB0_1421

.LBB0_1421:
	s_add_u32 s21, s21, s10
	s_addc_u32 s26, s26, s11
	s_add_u32 s20, s20, s16
	s_addc_u32 s27, s27, s17
	s_add_u32 s34, s34, s10
	s_waitcnt vmcnt(5)
	v_mov_b64_e32 v[8:9], v[16:17]
	s_waitcnt vmcnt(4)
	v_mov_b64_e32 v[4:5], v[12:13]
	s_addc_u32 s35, s35, s11
	v_lshl_add_u64 v[22:23], v[22:23], 0, s[22:23]
	s_andn2_b64 vcc, exec, s[24:25]
	v_mov_b32_e32 v1, v2
	v_mov_b64_e32 v[24:25], v[26:27]
	v_mov_b64_e32 v[10:11], v[18:19]
	v_mov_b64_e32 v[6:7], v[14:15]
	s_mov_b32 s18, s9
	s_cbranch_vccz .LBB0_1427
